# baseline (speedup 1.0000x reference)
.LBB3_6:
	v_lshlrev_b32_e32 v104, 3, v24
	v_or_b32_e32 v24, s18, v30
	v_mov_b32_e32 v25, s19
	v_lshlrev_b64 v[24:25], 12, v[24:25]
	v_lshl_add_u64 v[80:81], s[14:15], 0, v[24:25]
	v_lshrrev_b32_e32 v106, 2, v203
	v_lshlrev_b32_e32 v24, 1, v204
	v_bfe_u32 v25, v203, 2, 2
	s_and_b32 s7, s33, 3
	s_and_b32 s66, s33, 3
	s_lshr_b32 s67, s66, 1
	s_mul_i32 s67, s67, 0x2800
	s_lshl_b32 s66, s66, 13
	s_add_i32 s66, s66, s67
	s_add_i32 s66, s66, 0x8000
	s_lshl_b32 s7, s7, 13
	s_lshr_b32 s62, s33, 2
	s_lshl_b32 s62, s62, 16
	s_mov_b32 s63, 0
	s_lshr_b32 s64, s33, 2
	s_lshl_b32 s64, s64, 12
	s_add_i32 s65, s64, 0x8000
	v_bitop3_b32 v26, v24, v106, 3 bitop3:0x78
	v_bitop3_b32 v24, v24, v25, 1 bitop3:0x36
	s_cmp_lg_u32 0, -1
	v_lshlrev_b32_e32 v218, 4, v24
	v_bitop3_b32 v24, v30, v0, 15 bitop3:0x78
	s_cselect_b32 s0, 0, 0
	v_lshlrev_b32_e32 v28, 4, v24
	s_add_i32 s23, s0, s7
	v_lshl_add_u64 v[164:165], v[80:81], 0, v[28:29]
	s_mov_b64 s[0:1], 0x0
	v_and_b32_e32 v105, 15, v0
	v_lshl_add_u64 v[24:25], v[164:165], 0, s[0:1]
	v_lshl_add_u64 v[24:25], v[24:25], 0, s[62:63]
	s_add_i32 s36, s23, 0x14800
	s_add_i32 s54, s66, 0x0
	s_add_i32 m0, s54, s64
	s_nop 0
	global_load_lds_dwordx4 v[24:25], off nt
	v_bitop3_b32 v24, v30, v105, 4 bitop3:0x36
	v_lshlrev_b32_e32 v28, 4, v24
	v_lshl_add_u64 v[24:25], v[80:81], 0, v[28:29]
	s_mov_b64 s[8:9], 0x4000
	v_lshlrev_b32_e32 v217, 4, v26
	v_lshl_add_u64 v[26:27], v[24:25], 0, s[8:9]
	v_lshl_add_u64 v[26:27], v[26:27], 0, s[62:63]
	s_add_i32 s8, s23, 0x14c00
	s_add_i32 s54, s66, 0x400
	s_add_i32 m0, s54, s64
	s_nop 0
	global_load_lds_dwordx4 v[26:27], off nt
	v_bitop3_b32 v26, v30, v105, 8 bitop3:0x36
	v_lshlrev_b32_e32 v28, 4, v26
	v_lshl_add_u64 v[26:27], v[80:81], 0, v[28:29]
	s_mov_b64 s[14:15], 0x8000
	v_bitop3_b32 v28, v30, v105, 12 bitop3:0x36
	v_lshl_add_u64 v[82:83], v[26:27], 0, s[14:15]
	v_lshl_add_u64 v[82:83], v[82:83], 0, s[62:63]
	s_add_i32 s14, s23, 0x15000
	s_add_i32 s54, s66, 0x800
	s_add_i32 m0, s54, s64
	s_nop 0
	global_load_lds_dwordx4 v[82:83], off nt
	v_lshlrev_b32_e32 v28, 4, v28
	v_lshl_add_u64 v[28:29], v[80:81], 0, v[28:29]
	s_mov_b64 s[14:15], 0xc000
	v_lshl_add_u64 v[80:81], v[28:29], 0, s[14:15]
	v_lshl_add_u64 v[80:81], v[80:81], 0, s[62:63]
	s_add_i32 s14, s23, 0x15400
	s_add_i32 s54, s66, 0xc00
	s_add_i32 m0, s54, s64
	s_nop 0
	global_load_lds_dwordx4 v[80:81], off nt
	s_mov_b64 s[26:27], 0x10000
	s_add_i32 s26, s23, 0x15800
	s_mov_b64 s[28:29], 0x14000
	s_add_i32 s28, s23, 0x15c00
	s_mov_b64 s[30:31], 0x18000
	s_add_i32 s30, s23, 0x16000
	s_mov_b64 s[30:31], 0x1c000
	v_lshl_add_u32 v216, v203, 6, 0
	v_add_u32_e32 v216, s57, v216
	s_add_i32 s23, s23, 0x16400
	s_mov_b64 s[52:53], 0x100
	v_lshl_add_u64 v[224:225], v[164:165], 0, s[52:53]
	v_lshl_add_u64 v[224:225], v[224:225], 0, s[62:63]
	s_add_i32 s54, s36, 0x0
	s_add_i32 m0, s54, s65
	s_nop 0
	global_load_lds_dwordx4 v[224:225], off nt
	s_mov_b64 s[52:53], 0x4100
	v_lshl_add_u64 v[224:225], v[24:25], 0, s[52:53]
	v_lshl_add_u64 v[224:225], v[224:225], 0, s[62:63]
	s_add_i32 s54, s36, 0x400
	s_add_i32 m0, s54, s65
	s_nop 0
	global_load_lds_dwordx4 v[224:225], off nt
	s_mov_b64 s[52:53], 0x8100
	v_lshl_add_u64 v[224:225], v[26:27], 0, s[52:53]
	v_lshl_add_u64 v[224:225], v[224:225], 0, s[62:63]
	s_add_i32 s54, s36, 0x800
	s_add_i32 m0, s54, s65
	s_nop 0
	global_load_lds_dwordx4 v[224:225], off nt
	s_mov_b64 s[52:53], 0xc100
	v_lshl_add_u64 v[224:225], v[28:29], 0, s[52:53]
	v_lshl_add_u64 v[224:225], v[224:225], 0, s[62:63]
	s_add_i32 s54, s36, 0xc00
	s_add_i32 m0, s54, s65
	s_nop 0
	global_load_lds_dwordx4 v[224:225], off nt
	s_mov_b64 s[52:53], 0x200
	v_lshl_add_u64 v[224:225], v[164:165], 0, s[52:53]
	v_lshl_add_u64 v[224:225], v[224:225], 0, s[62:63]
	s_add_i32 s54, s36, 0x0
	s_add_i32 m0, s54, s64
	s_nop 0
	global_load_lds_dwordx4 v[224:225], off nt
	s_mov_b64 s[52:53], 0x4200
	v_lshl_add_u64 v[224:225], v[24:25], 0, s[52:53]
	v_lshl_add_u64 v[224:225], v[224:225], 0, s[62:63]
	s_add_i32 s54, s36, 0x400
	s_add_i32 m0, s54, s64
	s_nop 0
	global_load_lds_dwordx4 v[224:225], off nt
	s_mov_b64 s[52:53], 0x8200
	v_lshl_add_u64 v[224:225], v[26:27], 0, s[52:53]
	v_lshl_add_u64 v[224:225], v[224:225], 0, s[62:63]
	s_add_i32 s54, s36, 0x800
	s_add_i32 m0, s54, s64
	s_nop 0
	global_load_lds_dwordx4 v[224:225], off nt
	s_mov_b64 s[52:53], 0xc200
	v_lshl_add_u64 v[224:225], v[28:29], 0, s[52:53]
	v_lshl_add_u64 v[224:225], v[224:225], 0, s[62:63]
	s_add_i32 s54, s36, 0xc00
	s_add_i32 m0, s54, s64
	s_nop 0
	global_load_lds_dwordx4 v[224:225], off nt
	s_waitcnt vmcnt(0) lgkmcnt(0)
	s_barrier
	v_and_b32_e32 v226, 31, v0
	v_bfe_u32 v227, v0, 5, 1
	v_lshrrev_b32_e32 v228, 2, v226
	v_lshlrev_b32_e32 v228, 10, v228
	v_and_b32_e32 v229, 3, v226
	v_lshlrev_b32_e32 v229, 8, v229
	v_add3_u32 v230, s36, v228, v229
	v_add3_u32 v228, s66, v228, v229
	v_and_b32_e32 v231, 15, v226
	v_xor_b32_e32 v231, v231, v227
	v_lshlrev_b32_e32 v231, 4, v231
	v_mov_b32_e32 v232, v231
	v_add_u32_e32 v232, v230, v232
	v_mov_b32_e32 v240, v231
	v_add_u32_e32 v240, v228, v240
	v_xor_b32_e32 v241, 0x80, v231
	v_add_u32_e32 v241, v228, v241
	v_xor_b32_e32 v242, 0x20, v231
	v_add_u32_e32 v242, v228, v242
	v_xor_b32_e32 v243, 0xa0, v231
	v_add_u32_e32 v243, v228, v243
	v_xor_b32_e32 v244, 0x40, v231
	v_add_u32_e32 v244, v228, v244
	v_xor_b32_e32 v245, 0xc0, v231
	v_add_u32_e32 v245, v228, v245
	v_xor_b32_e32 v246, 0x60, v231
	v_add_u32_e32 v246, v228, v246
	v_xor_b32_e32 v247, 0xe0, v231
	v_add_u32_e32 v247, v228, v247
	ds_read_b128 v[64:67], v240
	v_xor_b32_e32 v233, 0x80, v231
	v_add_u32_e32 v233, v230, v233
	ds_read_b128 v[2:5], v241
	v_xor_b32_e32 v234, 0x20, v231
	v_add_u32_e32 v234, v230, v234
	ds_read_b128 v[68:71], v242
	v_xor_b32_e32 v235, 0xa0, v231
	v_add_u32_e32 v235, v230, v235
	ds_read_b128 v[6:9], v243
	v_xor_b32_e32 v236, 0x40, v231
	v_add_u32_e32 v236, v230, v236
	ds_read_b128 v[72:75], v244
	v_xor_b32_e32 v237, 0xc0, v231
	v_add_u32_e32 v237, v230, v237
	ds_read_b128 v[10:13], v245
	v_xor_b32_e32 v238, 0x60, v231
	v_add_u32_e32 v238, v230, v238
	ds_read_b128 v[76:79], v246
	v_xor_b32_e32 v239, 0xe0, v231
	v_add_u32_e32 v239, v230, v239
	ds_read_b128 v[14:17], v247
	s_waitcnt lgkmcnt(0)
	s_mov_b64 s[52:53], 0x10100
	s_add_i32 s54, s36, 0x1000
	s_mov_b64 s[52:53], 0x14100
	s_add_i32 s54, s36, 0x1400
	s_mov_b64 s[52:53], 0x18100
	s_add_i32 s54, s36, 0x1800
	s_mov_b64 s[52:53], 0x1c100
	s_add_i32 s54, s36, 0x1c00
	v_add_u32_e32 v209, v216, v217
	v_add_u32_e32 v210, v216, v218
	ds_read_b128 v[80:83], v209
	ds_read_b128 v[88:91], v209 offset:2048
	ds_read_b128 v[84:87], v210
	ds_read_b128 v[92:95], v210 offset:2048
	v_mov_b32_e32 v219, 0x7f7f7f7f
	v_mov_b32_e32 v220, 0x7c7c7c7c
	s_waitcnt vmcnt(10) lgkmcnt(1)
	v_mfma_scale_f32_32x32x64_f8f6f4 v[64:79], v[80:87], v[96:103], v[64:79], v219, v220 op_sel_hi:[0,0,0]
	s_waitcnt vmcnt(8) lgkmcnt(0)
	v_mfma_scale_f32_32x32x64_f8f6f4 v[2:17], v[88:95], v[96:103], v[2:17], v219, v220 op_sel_hi:[0,0,0]
	s_mov_b32 s39, 0x3fb8aa3b
	s_nop 15
	s_nop 15
	s_nop 15
	s_nop 15
	s_nop 15
	s_nop 15
	s_waitcnt vmcnt(0) lgkmcnt(0)
	s_barrier
	ds_read_b128 v[48:51], v232 offset:32768
	ds_read_b128 v[32:35], v233 offset:32768
	ds_read_b128 v[52:55], v234 offset:32768
	ds_read_b128 v[36:39], v235 offset:32768
	ds_read_b128 v[56:59], v236 offset:32768
	ds_read_b128 v[40:43], v237 offset:32768
	ds_read_b128 v[60:63], v238 offset:32768
	ds_read_b128 v[44:47], v239 offset:32768
	s_waitcnt lgkmcnt(0)
	v_lshlrev_b32_e32 v31, 2, v204
	v_max_f32_e32 v80, v65, v65
	v_max_f32_e32 v81, v64, v64
	v_max_f32_e32 v80, v81, v80
	v_max3_f32 v81, v66, v67, v3
	v_max3_f32 v80, v80, v2, v4
	v_max3_f32 v80, v80, v5, v68
	v_max3_f32 v81, v81, v70, v71
	v_max3_f32 v80, v80, v69, v6
	v_max3_f32 v81, v81, v8, v9
	v_max3_f32 v80, v80, v7, v72
	v_max3_f32 v81, v81, v74, v75
	v_max3_f32 v80, v80, v73, v10
	v_max3_f32 v81, v81, v12, v13
	v_max3_f32 v80, v80, v11, v76
	v_max3_f32 v81, v81, v78, v79
	v_max3_f32 v80, v80, v77, v14
	v_max3_f32 v81, v81, v16, v17
	v_max3_f32 v80, v80, v15, v81
	v_mov_b32_e32 v81, v80
	s_nop 1
	v_permlane32_swap_b32_e32 v80, v81
	v_max_f32_e32 v81, v81, v81
	v_max_f32_e32 v80, v80, v80
	v_max_f32_e32 v80, v80, v81
	v_mul_f32_e32 v208, 0x3fb8aa3b, v80
	s_mov_b32 s48, 0
	s_mov_b32 s38, -1
	s_mov_b64 s[0:1], 0x4000
	s_mov_b64 s[8:9], 0x8000
	s_mov_b64 s[24:25], 0xc000
	s_mov_b64 s[14:15], 0x10000
	s_mov_b64 s[26:27], 0x14000
	s_mov_b64 s[28:29], 0x18000
	s_mov_b64 s[30:31], 0x1c000
	v_fma_f32 v64, v64, s39, -v208
	v_fma_f32 v2, v2, s39, -v208
	v_fma_f32 v65, v65, s39, -v208
	v_fma_f32 v3, v3, s39, -v208
	v_fma_f32 v66, v66, s39, -v208
	v_fma_f32 v4, v4, s39, -v208
	v_fma_f32 v67, v67, s39, -v208
	v_fma_f32 v5, v5, s39, -v208
	v_fma_f32 v68, v68, s39, -v208
	v_fma_f32 v6, v6, s39, -v208
	v_fma_f32 v69, v69, s39, -v208
	v_fma_f32 v7, v7, s39, -v208
	v_fma_f32 v70, v70, s39, -v208
	v_fma_f32 v8, v8, s39, -v208
	v_fma_f32 v71, v71, s39, -v208
	v_fma_f32 v9, v9, s39, -v208
	v_fma_f32 v72, v72, s39, -v208
	v_fma_f32 v10, v10, s39, -v208
	v_fma_f32 v73, v73, s39, -v208
	v_fma_f32 v11, v11, s39, -v208
	v_fma_f32 v74, v74, s39, -v208
	v_fma_f32 v12, v12, s39, -v208
	v_fma_f32 v75, v75, s39, -v208
	v_fma_f32 v13, v13, s39, -v208
	v_fma_f32 v76, v76, s39, -v208
	v_fma_f32 v14, v14, s39, -v208
	v_fma_f32 v77, v77, s39, -v208
	v_fma_f32 v78, v78, s39, -v208
	v_fma_f32 v79, v79, s39, -v208
	v_fma_f32 v94, v15, s39, -v208
	v_fma_f32 v16, v16, s39, -v208
	v_fma_f32 v15, v17, s39, -v208
	s_and_b64 vcc, exec, s[4:5]
	s_nop 0
	s_mov_b64 s[42:43], 0x30000
	v_lshl_add_u64 v[22:23], v[22:23], 0, s[42:43]
	s_mov_b32 m0, s37
	s_nop 0
	global_load_lds_dwordx4 v[22:23], off

	.amdhsa_kernel _Z6k_attnILi1024ELi1024ELi1024ELi1024ELi3072ELi1024ELb1ELb1EEvPKDF16_S1_S1_PKfPDF16_
		.amdhsa_group_segment_fixed_size 0
		.amdhsa_private_segment_fixed_size 0
		.amdhsa_kernarg_size 40
		.amdhsa_user_sgpr_count 2
		.amdhsa_user_sgpr_dispatch_ptr 0
		.amdhsa_user_sgpr_queue_ptr 0
		.amdhsa_user_sgpr_kernarg_segment_ptr 1
		.amdhsa_user_sgpr_dispatch_id 0
		.amdhsa_user_sgpr_kernarg_preload_length 0
		.amdhsa_user_sgpr_kernarg_preload_offset 0
		.amdhsa_user_sgpr_private_segment_size 0
		.amdhsa_uses_dynamic_stack 0
		.amdhsa_enable_private_segment 0
		.amdhsa_system_sgpr_workgroup_id_x 1
		.amdhsa_system_sgpr_workgroup_id_y 0
		.amdhsa_system_sgpr_workgroup_id_z 0
		.amdhsa_system_sgpr_workgroup_info 0
		.amdhsa_system_vgpr_workitem_id 0
		.amdhsa_next_free_vgpr 248
		.amdhsa_next_free_sgpr 68
		.amdhsa_accum_offset 248
		.amdhsa_reserve_vcc 1
		.amdhsa_float_round_mode_32 0
		.amdhsa_float_round_mode_16_64 0
		.amdhsa_float_denorm_mode_32 3
		.amdhsa_float_denorm_mode_16_64 3
		.amdhsa_dx10_clamp 1
		.amdhsa_ieee_mode 1
		.amdhsa_fp16_overflow 0
		.amdhsa_tg_split 0
		.amdhsa_exception_fp_ieee_invalid_op 0
		.amdhsa_exception_fp_denorm_src 0
		.amdhsa_exception_fp_ieee_div_zero 0
		.amdhsa_exception_fp_ieee_overflow 0
		.amdhsa_exception_fp_ieee_underflow 0
		.amdhsa_exception_fp_ieee_inexact 0
		.amdhsa_exception_int_div_zero 0
	.end_amdhsa_kernel

.LBB6_6:
	v_lshlrev_b32_e32 v30, 3, v22
	v_or_b32_e32 v22, s18, v28
	v_mov_b32_e32 v23, s19
	v_lshlrev_b64 v[22:23], 13, v[22:23]
	v_lshl_add_u64 v[80:81], s[14:15], 0, v[22:23]
	v_lshrrev_b32_e32 v104, 2, v203
	v_lshlrev_b32_e32 v22, 1, v204
	v_bfe_u32 v23, v203, 2, 2
	s_and_b32 s7, s33, 3
	s_and_b32 s66, s33, 3
	s_lshr_b32 s67, s66, 1
	s_mul_i32 s67, s67, 0x2800
	s_lshl_b32 s66, s66, 13
	s_add_i32 s66, s66, s67
	s_add_i32 s66, s66, 0x8000
	s_lshl_b32 s7, s7, 13
	s_lshr_b32 s62, s33, 2
	s_lshl_b32 s62, s62, 17
	s_mov_b32 s63, 0
	s_lshr_b32 s64, s33, 2
	s_lshl_b32 s64, s64, 12
	s_add_i32 s65, s64, 0x8000
	v_bitop3_b32 v24, v22, v104, 3 bitop3:0x78
	v_bitop3_b32 v22, v22, v23, 1 bitop3:0x36
	s_cmp_lg_u32 0, -1
	v_lshlrev_b32_e32 v218, 4, v22
	v_bitop3_b32 v22, v28, v0, 15 bitop3:0x78
	s_cselect_b32 s0, 0, 0
	v_lshlrev_b32_e32 v26, 4, v22
	s_add_i32 s41, s0, s7
	v_lshl_add_u64 v[164:165], v[80:81], 0, v[26:27]
	s_mov_b64 s[0:1], 0x0
	v_and_b32_e32 v31, 15, v0
	v_lshl_add_u64 v[22:23], v[164:165], 0, s[0:1]
	v_lshl_add_u64 v[22:23], v[22:23], 0, s[62:63]
	s_add_i32 s38, s41, 0x14800
	s_add_i32 s54, s66, 0x0
	s_add_i32 m0, s54, s64
	s_nop 0
	global_load_lds_dwordx4 v[22:23], off nt
	v_bitop3_b32 v22, v28, v31, 4 bitop3:0x36
	v_lshlrev_b32_e32 v26, 4, v22
	v_lshl_add_u64 v[22:23], v[80:81], 0, v[26:27]
	s_mov_b64 s[8:9], 0x8000
	v_lshlrev_b32_e32 v217, 4, v24
	v_lshl_add_u64 v[24:25], v[22:23], 0, s[8:9]
	v_lshl_add_u64 v[24:25], v[24:25], 0, s[62:63]
	s_add_i32 s8, s41, 0x14c00
	s_add_i32 s54, s66, 0x400
	s_add_i32 m0, s54, s64
	s_nop 0
	global_load_lds_dwordx4 v[24:25], off nt
	v_bitop3_b32 v24, v28, v31, 8 bitop3:0x36
	v_lshlrev_b32_e32 v26, 4, v24
	v_lshl_add_u64 v[24:25], v[80:81], 0, v[26:27]
	s_mov_b64 s[8:9], 0x10000
	v_bitop3_b32 v26, v28, v31, 12 bitop3:0x36
	v_lshl_add_u64 v[82:83], v[24:25], 0, s[8:9]
	v_lshl_add_u64 v[82:83], v[82:83], 0, s[62:63]
	s_add_i32 s8, s41, 0x15000
	s_add_i32 s54, s66, 0x800
	s_add_i32 m0, s54, s64
	s_nop 0
	global_load_lds_dwordx4 v[82:83], off nt
	v_lshlrev_b32_e32 v26, 4, v26
	v_lshl_add_u64 v[26:27], v[80:81], 0, v[26:27]
	s_mov_b64 s[8:9], 0x18000
	v_lshl_add_u64 v[80:81], v[26:27], 0, s[8:9]
	v_lshl_add_u64 v[80:81], v[80:81], 0, s[62:63]
	s_add_i32 s8, s41, 0x15400
	s_add_i32 s54, s66, 0xc00
	s_add_i32 m0, s54, s64
	s_nop 0
	global_load_lds_dwordx4 v[80:81], off nt
	s_mov_b64 s[14:15], 0x20000
	s_add_i32 s14, s41, 0x15800
	s_mov_b64 s[14:15], 0x28000
	s_add_i32 s14, s41, 0x15c00
	s_mov_b64 s[34:35], 0x30000
	s_add_i32 s34, s41, 0x16000
	s_mov_b64 s[34:35], 0x38000
	v_lshl_add_u32 v216, v203, 6, 0
	v_add_u32_e32 v216, s57, v216
	s_add_i32 s41, s41, 0x16400
	s_mov_b64 s[52:53], 0x100
	v_lshl_add_u64 v[224:225], v[164:165], 0, s[52:53]
	v_lshl_add_u64 v[224:225], v[224:225], 0, s[62:63]
	s_add_i32 s54, s38, 0x0
	s_add_i32 m0, s54, s65
	s_nop 0
	global_load_lds_dwordx4 v[224:225], off nt
	s_mov_b64 s[52:53], 0x8100
	v_lshl_add_u64 v[224:225], v[22:23], 0, s[52:53]
	v_lshl_add_u64 v[224:225], v[224:225], 0, s[62:63]
	s_add_i32 s54, s38, 0x400
	s_add_i32 m0, s54, s65
	s_nop 0
	global_load_lds_dwordx4 v[224:225], off nt
	s_mov_b64 s[52:53], 0x10100
	v_lshl_add_u64 v[224:225], v[24:25], 0, s[52:53]
	v_lshl_add_u64 v[224:225], v[224:225], 0, s[62:63]
	s_add_i32 s54, s38, 0x800
	s_add_i32 m0, s54, s65
	s_nop 0
	global_load_lds_dwordx4 v[224:225], off nt
	s_mov_b64 s[52:53], 0x18100
	v_lshl_add_u64 v[224:225], v[26:27], 0, s[52:53]
	v_lshl_add_u64 v[224:225], v[224:225], 0, s[62:63]
	s_add_i32 s54, s38, 0xc00
	s_add_i32 m0, s54, s65
	s_nop 0
	global_load_lds_dwordx4 v[224:225], off nt
	s_mov_b64 s[52:53], 0x200
	v_lshl_add_u64 v[224:225], v[164:165], 0, s[52:53]
	v_lshl_add_u64 v[224:225], v[224:225], 0, s[62:63]
	s_add_i32 s54, s38, 0x0
	s_add_i32 m0, s54, s64
	s_nop 0
	global_load_lds_dwordx4 v[224:225], off nt
	s_mov_b64 s[52:53], 0x8200
	v_lshl_add_u64 v[224:225], v[22:23], 0, s[52:53]
	v_lshl_add_u64 v[224:225], v[224:225], 0, s[62:63]
	s_add_i32 s54, s38, 0x400
	s_add_i32 m0, s54, s64
	s_nop 0
	global_load_lds_dwordx4 v[224:225], off nt
	s_mov_b64 s[52:53], 0x10200
	v_lshl_add_u64 v[224:225], v[24:25], 0, s[52:53]
	v_lshl_add_u64 v[224:225], v[224:225], 0, s[62:63]
	s_add_i32 s54, s38, 0x800
	s_add_i32 m0, s54, s64
	s_nop 0
	global_load_lds_dwordx4 v[224:225], off nt
	s_mov_b64 s[52:53], 0x18200
	v_lshl_add_u64 v[224:225], v[26:27], 0, s[52:53]
	v_lshl_add_u64 v[224:225], v[224:225], 0, s[62:63]
	s_add_i32 s54, s38, 0xc00
	s_add_i32 m0, s54, s64
	s_nop 0
	global_load_lds_dwordx4 v[224:225], off nt
	s_waitcnt vmcnt(0) lgkmcnt(0)
	s_barrier
	v_and_b32_e32 v226, 31, v0
	v_bfe_u32 v227, v0, 5, 1
	v_lshrrev_b32_e32 v228, 2, v226
	v_lshlrev_b32_e32 v228, 10, v228
	v_and_b32_e32 v229, 3, v226
	v_lshlrev_b32_e32 v229, 8, v229
	v_add3_u32 v230, s38, v228, v229
	v_add3_u32 v228, s66, v228, v229
	v_and_b32_e32 v231, 15, v226
	v_xor_b32_e32 v231, v231, v227
	v_lshlrev_b32_e32 v231, 4, v231
	v_mov_b32_e32 v232, v231
	v_add_u32_e32 v232, v230, v232
	v_mov_b32_e32 v240, v231
	v_add_u32_e32 v240, v228, v240
	v_xor_b32_e32 v241, 0x80, v231
	v_add_u32_e32 v241, v228, v241
	v_xor_b32_e32 v242, 0x20, v231
	v_add_u32_e32 v242, v228, v242
	v_xor_b32_e32 v243, 0xa0, v231
	v_add_u32_e32 v243, v228, v243
	v_xor_b32_e32 v244, 0x40, v231
	v_add_u32_e32 v244, v228, v244
	v_xor_b32_e32 v245, 0xc0, v231
	v_add_u32_e32 v245, v228, v245
	v_xor_b32_e32 v246, 0x60, v231
	v_add_u32_e32 v246, v228, v246
	v_xor_b32_e32 v247, 0xe0, v231
	v_add_u32_e32 v247, v228, v247
	ds_read_b128 v[64:67], v240
	v_xor_b32_e32 v233, 0x80, v231
	v_add_u32_e32 v233, v230, v233
	ds_read_b128 v[2:5], v241
	v_xor_b32_e32 v234, 0x20, v231
	v_add_u32_e32 v234, v230, v234
	ds_read_b128 v[68:71], v242
	v_xor_b32_e32 v235, 0xa0, v231
	v_add_u32_e32 v235, v230, v235
	ds_read_b128 v[6:9], v243
	v_xor_b32_e32 v236, 0x40, v231
	v_add_u32_e32 v236, v230, v236
	ds_read_b128 v[72:75], v244
	v_xor_b32_e32 v237, 0xc0, v231
	v_add_u32_e32 v237, v230, v237
	ds_read_b128 v[10:13], v245
	v_xor_b32_e32 v238, 0x60, v231
	v_add_u32_e32 v238, v230, v238
	ds_read_b128 v[76:79], v246
	v_xor_b32_e32 v239, 0xe0, v231
	v_add_u32_e32 v239, v230, v239
	ds_read_b128 v[14:17], v247
	s_waitcnt lgkmcnt(0)
	s_mov_b64 s[52:53], 0x20100
	s_add_i32 s54, s38, 0x1000
	s_mov_b64 s[52:53], 0x28100
	s_add_i32 s54, s38, 0x1400
	s_mov_b64 s[52:53], 0x30100
	s_add_i32 s54, s38, 0x1800
	s_mov_b64 s[52:53], 0x38100
	s_add_i32 s54, s38, 0x1c00
	v_add_u32_e32 v209, v216, v217
	v_add_u32_e32 v210, v216, v218
	ds_read_b128 v[80:83], v209
	ds_read_b128 v[88:91], v209 offset:2048
	ds_read_b128 v[84:87], v210
	ds_read_b128 v[92:95], v210 offset:2048
	v_mov_b32_e32 v219, 0x7f7f7f7f
	v_mov_b32_e32 v220, 0x7c7c7c7c
	s_waitcnt vmcnt(10) lgkmcnt(1)
	v_mfma_scale_f32_32x32x64_f8f6f4 v[64:79], v[80:87], v[96:103], v[64:79], v219, v220 op_sel_hi:[0,0,0]
	s_waitcnt vmcnt(8) lgkmcnt(0)
	v_mfma_scale_f32_32x32x64_f8f6f4 v[2:17], v[88:95], v[96:103], v[2:17], v219, v220 op_sel_hi:[0,0,0]
	s_mov_b32 s41, 0x3fb8aa3b
	s_nop 15
	s_nop 15
	s_nop 15
	s_nop 15
	s_nop 15
	s_nop 15
	s_waitcnt vmcnt(0) lgkmcnt(0)
	s_barrier
	ds_read_b128 v[48:51], v232 offset:32768
	ds_read_b128 v[32:35], v233 offset:32768
	ds_read_b128 v[52:55], v234 offset:32768
	ds_read_b128 v[36:39], v235 offset:32768
	ds_read_b128 v[56:59], v236 offset:32768
	ds_read_b128 v[40:43], v237 offset:32768
	ds_read_b128 v[60:63], v238 offset:32768
	ds_read_b128 v[44:47], v239 offset:32768
	s_waitcnt lgkmcnt(0)
	v_lshlrev_b32_e32 v29, 2, v204
	v_max_f32_e32 v80, v65, v65
	v_max_f32_e32 v81, v64, v64
	v_max_f32_e32 v80, v81, v80
	v_max3_f32 v81, v66, v67, v3
	v_max3_f32 v80, v80, v2, v4
	v_max3_f32 v80, v80, v5, v68
	v_max3_f32 v81, v81, v70, v71
	v_max3_f32 v80, v80, v69, v6
	v_max3_f32 v81, v81, v8, v9
	v_max3_f32 v80, v80, v7, v72
	v_max3_f32 v81, v81, v74, v75
	v_max3_f32 v80, v80, v73, v10
	v_max3_f32 v81, v81, v12, v13
	v_max3_f32 v80, v80, v11, v76
	v_max3_f32 v81, v81, v78, v79
	v_max3_f32 v80, v80, v77, v14
	v_max3_f32 v81, v81, v16, v17
	v_max3_f32 v80, v80, v15, v81
	v_mov_b32_e32 v81, v80
	s_nop 1
	v_permlane32_swap_b32_e32 v80, v81
	v_max_f32_e32 v81, v81, v81
	v_max_f32_e32 v80, v80, v80
	v_max_f32_e32 v80, v80, v81
	v_mul_f32_e32 v208, 0x3fb8aa3b, v80
	s_mov_b32 s27, 0
	s_mov_b32 s40, -1
	s_mov_b64 s[0:1], 0x8000
	s_mov_b64 s[28:29], 0x10000
	s_mov_b64 s[20:21], 0x18000
	s_mov_b64 s[8:9], 0x20000
	s_mov_b64 s[30:31], 0x28000
	s_mov_b64 s[14:15], 0x30000
	s_mov_b64 s[34:35], 0x38000
	v_fma_f32 v64, v64, s41, -v208
	v_fma_f32 v2, v2, s41, -v208
	v_fma_f32 v65, v65, s41, -v208
	v_fma_f32 v3, v3, s41, -v208
	v_fma_f32 v66, v66, s41, -v208
	v_fma_f32 v4, v4, s41, -v208
	v_fma_f32 v67, v67, s41, -v208
	v_fma_f32 v5, v5, s41, -v208
	v_fma_f32 v68, v68, s41, -v208
	v_fma_f32 v6, v6, s41, -v208
	v_fma_f32 v69, v69, s41, -v208
	v_fma_f32 v7, v7, s41, -v208
	v_fma_f32 v70, v70, s41, -v208
	v_fma_f32 v8, v8, s41, -v208
	v_fma_f32 v71, v71, s41, -v208
	v_fma_f32 v9, v9, s41, -v208
	v_fma_f32 v72, v72, s41, -v208
	v_fma_f32 v10, v10, s41, -v208
	v_fma_f32 v73, v73, s41, -v208
	v_fma_f32 v11, v11, s41, -v208
	v_fma_f32 v74, v74, s41, -v208
	v_fma_f32 v12, v12, s41, -v208
	v_fma_f32 v75, v75, s41, -v208
	v_fma_f32 v13, v13, s41, -v208
	v_fma_f32 v76, v76, s41, -v208
	v_fma_f32 v14, v14, s41, -v208
	v_fma_f32 v77, v77, s41, -v208
	v_fma_f32 v78, v78, s41, -v208
	v_fma_f32 v79, v79, s41, -v208
	v_fma_f32 v94, v15, s41, -v208
	v_fma_f32 v16, v16, s41, -v208
	v_fma_f32 v15, v17, s41, -v208
	s_and_b64 vcc, exec, s[4:5]
	s_nop 0
	v_lshl_add_u64 v[20:21], v[20:21], 0, s[14:15]
	s_mov_b32 m0, s39
	s_nop 0
	global_load_lds_dwordx4 v[20:21], off

	.amdhsa_kernel _Z6k_attnILi1024ELi2048ELi1024ELi1024ELi2048ELi1024ELb1ELb1EEvPKDF16_S1_S1_PKfPDF16_
		.amdhsa_group_segment_fixed_size 0
		.amdhsa_private_segment_fixed_size 0
		.amdhsa_kernarg_size 40
		.amdhsa_user_sgpr_count 2
		.amdhsa_user_sgpr_dispatch_ptr 0
		.amdhsa_user_sgpr_queue_ptr 0
		.amdhsa_user_sgpr_kernarg_segment_ptr 1
		.amdhsa_user_sgpr_dispatch_id 0
		.amdhsa_user_sgpr_kernarg_preload_length 0
		.amdhsa_user_sgpr_kernarg_preload_offset 0
		.amdhsa_user_sgpr_private_segment_size 0
		.amdhsa_uses_dynamic_stack 0
		.amdhsa_enable_private_segment 0
		.amdhsa_system_sgpr_workgroup_id_x 1
		.amdhsa_system_sgpr_workgroup_id_y 0
		.amdhsa_system_sgpr_workgroup_id_z 0
		.amdhsa_system_sgpr_workgroup_info 0
		.amdhsa_system_vgpr_workitem_id 0
		.amdhsa_next_free_vgpr 248
		.amdhsa_next_free_sgpr 68
		.amdhsa_accum_offset 248
		.amdhsa_reserve_vcc 1
		.amdhsa_float_round_mode_32 0
		.amdhsa_float_round_mode_16_64 0
		.amdhsa_float_denorm_mode_32 3
		.amdhsa_float_denorm_mode_16_64 3
		.amdhsa_dx10_clamp 1
		.amdhsa_ieee_mode 1
		.amdhsa_fp16_overflow 0
		.amdhsa_tg_split 0
		.amdhsa_exception_fp_ieee_invalid_op 0
		.amdhsa_exception_fp_denorm_src 0
		.amdhsa_exception_fp_ieee_div_zero 0
		.amdhsa_exception_fp_ieee_overflow 0
		.amdhsa_exception_fp_ieee_underflow 0
		.amdhsa_exception_fp_ieee_inexact 0
		.amdhsa_exception_int_div_zero 0
	.end_amdhsa_kernel

amdhsa.kernels:
  - .agpr_count:     0
    .args:
      - .offset:         0
        .size:           384
        .value_kind:     by_value
    .group_segment_fixed_size: 5120
    .kernarg_segment_align: 8
    .kernarg_segment_size: 384
    .language:       OpenCL C
    .language_version:
      - 2
      - 0
    .max_flat_workgroup_size: 256
    .name:           _Z6k_prep6WtArgs
    .private_segment_fixed_size: 0
    .sgpr_count:     38
    .sgpr_spill_count: 0
    .symbol:         _Z6k_prep6WtArgs.kd
    .uniform_work_group_size: 1
    .uses_dynamic_stack: false
    .vgpr_count:     29
    .vgpr_spill_count: 0
    .wavefront_size: 64
  - .agpr_count:     0
    .args:
      - .actual_access:  read_only
        .address_space:  global
        .offset:         0
        .size:           8
        .value_kind:     global_buffer
      - .actual_access:  read_only
        .address_space:  global
        .offset:         8
        .size:           8
        .value_kind:     global_buffer
      - .actual_access:  read_only
        .address_space:  global
        .offset:         16
        .size:           8
        .value_kind:     global_buffer
      - .actual_access:  write_only
        .address_space:  global
        .offset:         24
        .size:           8
        .value_kind:     global_buffer
      - .actual_access:  write_only
        .address_space:  global
        .offset:         32
        .size:           8
        .value_kind:     global_buffer
      - .actual_access:  write_only
        .address_space:  global
        .offset:         40
        .size:           8
        .value_kind:     global_buffer
      - .offset:         48
        .size:           4
        .value_kind:     by_value
    .group_segment_fixed_size: 0
    .kernarg_segment_align: 8
    .kernarg_segment_size: 52
    .language:       OpenCL C
    .language_version:
      - 2
      - 0
    .max_flat_workgroup_size: 256
    .name:           _Z4k_lnPKDF16_PKfS2_PfPDF16_Phi
    .private_segment_fixed_size: 0
    .sgpr_count:     18
    .sgpr_spill_count: 0
    .symbol:         _Z4k_lnPKDF16_PKfS2_PfPDF16_Phi.kd
    .uniform_work_group_size: 1
    .uses_dynamic_stack: false
    .vgpr_count:     59
    .vgpr_spill_count: 0
    .wavefront_size: 64
  - .agpr_count:     0
    .args:
      - .offset:         0
        .size:           56
        .value_kind:     by_value
      - .offset:         56
        .size:           72
        .value_kind:     by_value
      - .offset:         128
        .size:           176
        .value_kind:     by_value
      - .address_space:  global
        .offset:         304
        .size:           8
        .value_kind:     global_buffer
      - .offset:         312
        .size:           4
        .value_kind:     hidden_block_count_x
      - .offset:         316
        .size:           4
        .value_kind:     hidden_block_count_y
      - .offset:         320
        .size:           4
        .value_kind:     hidden_block_count_z
      - .offset:         324
        .size:           2
        .value_kind:     hidden_group_size_x
      - .offset:         326
        .size:           2
        .value_kind:     hidden_group_size_y
      - .offset:         328
        .size:           2
        .value_kind:     hidden_group_size_z
      - .offset:         330
        .size:           2
        .value_kind:     hidden_remainder_x
      - .offset:         332
        .size:           2
        .value_kind:     hidden_remainder_y
      - .offset:         334
        .size:           2
        .value_kind:     hidden_remainder_z
      - .offset:         352
        .size:           8
        .value_kind:     hidden_global_offset_x
      - .offset:         360
        .size:           8
        .value_kind:     hidden_global_offset_y
      - .offset:         368
        .size:           8
        .value_kind:     hidden_global_offset_z
      - .offset:         376
        .size:           2
        .value_kind:     hidden_grid_dims
      - .offset:         432
        .size:           4
        .value_kind:     hidden_dynamic_lds_size
    .group_segment_fixed_size: 0
    .kernarg_segment_align: 8
    .kernarg_segment_size: 568
    .language:       OpenCL C
    .language_version:
      - 2
      - 0
    .max_flat_workgroup_size: 512
    .name:           _Z6k_gemmIN3pg84EpiHILi0ELb1EEELb1EEvNS0_4GemmET_6WtTailPj
    .private_segment_fixed_size: 0
    .sgpr_count:     74
    .sgpr_spill_count: 5
    .symbol:         _Z6k_gemmIN3pg84EpiHILi0ELb1EEELb1EEvNS0_4GemmET_6WtTailPj.kd
    .uniform_work_group_size: 1
    .uses_dynamic_stack: false
    .vgpr_count:     248
    .vgpr_spill_count: 0
    .wavefront_size: 64
  - .agpr_count:     0
    .args:
      - .address_space:  global
        .offset:         0
        .size:           8
        .value_kind:     global_buffer
      - .address_space:  global
        .offset:         8
        .size:           8
        .value_kind:     global_buffer
      - .address_space:  global
        .offset:         16
        .size:           8
        .value_kind:     global_buffer
      - .address_space:  global
        .offset:         24
        .size:           8
        .value_kind:     global_buffer
      - .address_space:  global
        .offset:         32
        .size:           8
        .value_kind:     global_buffer
    .group_segment_fixed_size: 0
    .kernarg_segment_align: 8
    .kernarg_segment_size: 40
    .language:       OpenCL C
    .language_version:
      - 2
      - 0
    .max_flat_workgroup_size: 512
    .name:           _Z6k_attnILi1024ELi1024ELi1024ELi1024ELi3072ELi1024ELb1ELb1EEvPKDF16_S1_S1_PKfPDF16_
    .private_segment_fixed_size: 0
    .sgpr_count:     55
    .sgpr_spill_count: 0
    .symbol:         _Z6k_attnILi1024ELi1024ELi1024ELi1024ELi3072ELi1024ELb1ELb1EEvPKDF16_S1_S1_PKfPDF16_.kd
    .uniform_work_group_size: 1
    .uses_dynamic_stack: false
    .vgpr_count:     224
    .vgpr_spill_count: 0
    .wavefront_size: 64
  - .agpr_count:     0
    .args:
      - .address_space:  global
        .offset:         0
        .size:           8
        .value_kind:     global_buffer
      - .address_space:  global
        .offset:         8
        .size:           8
        .value_kind:     global_buffer
      - .offset:         16
        .size:           4
        .value_kind:     by_value
      - .offset:         20
        .size:           4
        .value_kind:     by_value
      - .offset:         24
        .size:           4
        .value_kind:     by_value
      - .offset:         32
        .size:           32
        .value_kind:     by_value
    .group_segment_fixed_size: 0
    .kernarg_segment_align: 8
    .kernarg_segment_size: 64
    .language:       OpenCL C
    .language_version:
      - 2
      - 0
    .max_flat_workgroup_size: 512
    .name:           _ZN2g811k_gemm128f8INS_6EpiResEEEvPKhS3_iiiT_
    .private_segment_fixed_size: 0
    .sgpr_count:     34
    .sgpr_spill_count: 0
    .symbol:         _ZN2g811k_gemm128f8INS_6EpiResEEEvPKhS3_iiiT_.kd
    .uniform_work_group_size: 1
    .uses_dynamic_stack: false
    .vgpr_count:     98
    .vgpr_spill_count: 0
    .wavefront_size: 64
  - .agpr_count:     0
    .args:
      - .address_space:  global
        .offset:         0
        .size:           8
        .value_kind:     global_buffer
      - .address_space:  global
        .offset:         8
        .size:           8
        .value_kind:     global_buffer
      - .offset:         16
        .size:           4
        .value_kind:     by_value
      - .offset:         20
        .size:           4
        .value_kind:     by_value
      - .offset:         24
        .size:           4
        .value_kind:     by_value
      - .offset:         32
        .size:           16
        .value_kind:     by_value
    .group_segment_fixed_size: 0
    .kernarg_segment_align: 8
    .kernarg_segment_size: 48
    .language:       OpenCL C
    .language_version:
      - 2
      - 0
    .max_flat_workgroup_size: 512
    .name:           _ZN2g811k_gemm128f8INS_5EpiQ8EEEvPKhS3_iiiT_
    .private_segment_fixed_size: 0
    .sgpr_count:     74
    .sgpr_spill_count: 0
    .symbol:         _ZN2g811k_gemm128f8INS_5EpiQ8EEEvPKhS3_iiiT_.kd
    .uniform_work_group_size: 1
    .uses_dynamic_stack: false
    .vgpr_count:     248
    .vgpr_spill_count: 0
    .wavefront_size: 64
  - .agpr_count:     0
    .args:
      - .address_space:  global
        .offset:         0
        .size:           8
        .value_kind:     global_buffer
      - .address_space:  global
        .offset:         8
        .size:           8
        .value_kind:     global_buffer
      - .address_space:  global
        .offset:         16
        .size:           8
        .value_kind:     global_buffer
      - .address_space:  global
        .offset:         24
        .size:           8
        .value_kind:     global_buffer
      - .address_space:  global
        .offset:         32
        .size:           8
        .value_kind:     global_buffer
    .group_segment_fixed_size: 0
    .kernarg_segment_align: 8
    .kernarg_segment_size: 40
    .language:       OpenCL C
    .language_version:
      - 2
      - 0
    .max_flat_workgroup_size: 512
    .name:           _Z6k_attnILi1024ELi2048ELi1024ELi1024ELi2048ELi1024ELb1ELb1EEvPKDF16_S1_S1_PKfPDF16_
    .private_segment_fixed_size: 0
    .sgpr_count:     52
    .sgpr_spill_count: 0
    .symbol:         _Z6k_attnILi1024ELi2048ELi1024ELi1024ELi2048ELi1024ELb1ELb1EEvPKDF16_S1_S1_PKfPDF16_.kd
    .uniform_work_group_size: 1
    .uses_dynamic_stack: false
    .vgpr_count:     224
    .vgpr_spill_count: 0
    .wavefront_size: 64
  - .agpr_count:     0
    .args:
      - .offset:         0
        .size:           56
        .value_kind:     by_value
      - .offset:         56
        .size:           72
        .value_kind:     by_value
      - .offset:         128
        .size:           176
        .value_kind:     by_value
      - .address_space:  global
        .offset:         304
        .size:           8
        .value_kind:     global_buffer
      - .offset:         312
        .size:           4
        .value_kind:     hidden_block_count_x
      - .offset:         316
        .size:           4
        .value_kind:     hidden_block_count_y
      - .offset:         320
        .size:           4
        .value_kind:     hidden_block_count_z
      - .offset:         324
        .size:           2
        .value_kind:     hidden_group_size_x
      - .offset:         326
        .size:           2
        .value_kind:     hidden_group_size_y
      - .offset:         328
        .size:           2
        .value_kind:     hidden_group_size_z
      - .offset:         330
        .size:           2
        .value_kind:     hidden_remainder_x
      - .offset:         332
        .size:           2
        .value_kind:     hidden_remainder_y
      - .offset:         334
        .size:           2
        .value_kind:     hidden_remainder_z
      - .offset:         352
        .size:           8
        .value_kind:     hidden_global_offset_x
      - .offset:         360
        .size:           8
        .value_kind:     hidden_global_offset_y
      - .offset:         368
        .size:           8
        .value_kind:     hidden_global_offset_z
      - .offset:         376
        .size:           2
        .value_kind:     hidden_grid_dims
      - .offset:         432
        .size:           4
        .value_kind:     hidden_dynamic_lds_size
    .group_segment_fixed_size: 0
    .kernarg_segment_align: 8
    .kernarg_segment_size: 568
    .language:       OpenCL C
    .language_version:
      - 2
      - 0
    .max_flat_workgroup_size: 512
    .name:           _Z6k_gemmIN3pg84EpiHILi1ELb0EEELb0EEvNS0_4GemmET_6WtTailPj
    .private_segment_fixed_size: 0
    .sgpr_count:     85
    .sgpr_spill_count: 0
    .symbol:         _Z6k_gemmIN3pg84EpiHILi1ELb0EEELb0EEvNS0_4GemmET_6WtTailPj.kd
    .uniform_work_group_size: 1
    .uses_dynamic_stack: false
    .vgpr_count:     242
    .vgpr_spill_count: 0
    .wavefront_size: 64
  - .agpr_count:     0
    .args:
      - .address_space:  global
        .offset:         0
        .size:           8
        .value_kind:     global_buffer
      - .address_space:  global
        .offset:         8
        .size:           8
        .value_kind:     global_buffer
      - .offset:         16
        .size:           4
        .value_kind:     by_value
      - .offset:         20
        .size:           4
        .value_kind:     by_value
      - .offset:         24
        .size:           4
        .value_kind:     by_value
      - .offset:         32
        .size:           32
        .value_kind:     by_value
    .group_segment_fixed_size: 0
    .kernarg_segment_align: 8
    .kernarg_segment_size: 64
    .language:       OpenCL C
    .language_version:
      - 2
      - 0
    .max_flat_workgroup_size: 512
    .name:           _ZN4g1289k_gemm128INS_8EpiRes16EEEvPKDF16_S3_iiiT_
    .private_segment_fixed_size: 0
    .sgpr_count:     35
    .sgpr_spill_count: 0
    .symbol:         _ZN4g1289k_gemm128INS_8EpiRes16EEEvPKDF16_S3_iiiT_.kd
    .uniform_work_group_size: 1
    .uses_dynamic_stack: false
    .vgpr_count:     112
    .vgpr_spill_count: 0
    .wavefront_size: 64
